# s12 + x3 prologue de-serialisation: all item loads issued before the first wait; the two lane scans run under them on prologue-dead registers
# speedup vs baseline: 1.0160x; 1.0074x over previous
; __device__ __forceinline__ void x3_wave(int item, int b0, const h16* __restrict__ proj, const float* __restrict__ small, const h16* __restrict__ qkc, const h16* __restrict__ CS, ...
;     ...
;     const int c = item & 31, hh = (item >> 5) & 3, bl = item >> 7;
;     const size_t row0 = (size_t)bl * SEQ + c * 64;
;     const int gbh = (b0 + bl) * 4 + hh, lbh = bl * 4 + hh;
;     const h16* cprev = CS + ((size_t)lbh * 32 + c) * 8192;
;     typedef __attribute__((address_space(3))) const f32x4 lds_cf32x4;
;     s16x8 qr[4], kA[4], kB[4];
;     {   const float* sp = small + ((size_t)b0 * SEQ + row0 + lane) * 16;
;         const float li = sp[8 + hh], lf = sp[12 + hh], Mc = Ms[gbh * 32 + c];
;         const float nsv = ns[((size_t)gbh * 32 + c) * 64 + lane];
;         const h16* vp = proj + row0 * PP + PC_CV + hh * 128 + (size_t)(lane >> 2) * PP + (lane & 3) * 8;
;         h16x8 xv[4][4];
; #pragma unroll
;         for (int sg = 0; sg < 4; ++sg)
; #pragma unroll
;             for (int vb = 0; vb < 4; ++vb) xv[sg][vb] = *(const h16x8*)(vp + (size_t)(16 * sg) * PP + 32 * vb);
;         {   const int r32 = lane & 31, hi = lane >> 5;
; #pragma unroll
;             for (int ks = 0; ks < 4; ++ks) { qr[ks] = *(const s16x8*)(qkc + (row0 + r32) * 512 + hh * 64 + 16 * ks + 8 * hi);
;                 kA[ks] = *(const s16x8*)(qkc + (row0 + r32) * 512 + 256 + hh * 64 + 16 * ks + 8 * hi); kB[ks] = kA[ks]; }
;         }
.LBB0_429:
	s_ashr_i32 s12, s4, 7
	s_and_b32 s6, s4, 31
	s_ashr_i32 s13, s12, 31
	s_lshl_b64 s[2:3], s[12:13], 11
	s_lshl_b32 s0, s6, 6
	s_bfe_u32 s10, s4, 0x20005
	s_or_b32 s2, s2, s0
	v_readlane_b32 s0, v255, 44
	s_lshl_b32 s1, s12, 2
	s_add_i32 s0, s12, s0
	s_or_b32 s12, s1, s10
	s_lshl_b32 s0, s0, 2
	s_ashr_i32 s13, s12, 31
	s_or_b32 s0, s0, s10
	s_lshl_b64 s[14:15], s[12:13], 19
	s_lshl_b32 s11, s6, 14
	v_readlane_b32 s1, v255, 43
	v_mov_b32_e32 v230, v250
	s_add_u32 s12, s2, s1
	s_addc_u32 s13, s3, 0
	v_ashrrev_i32_e32 v231, 31, v230
	v_lshl_add_u64 v[0:1], s[12:13], 0, v[230:231]
	v_lshlrev_b64 v[0:1], 6, v[0:1]
	v_lshl_add_u64 v[0:1], s[86:87], 0, v[0:1]
	s_lshl_b32 s28, s10, 2
	v_lshl_add_u64 v[4:5], v[0:1], 0, s[28:29]
	global_load_dword v210, v[4:5], off offset:48
	s_lshl_b32 s1, s0, 5
	s_or_b32 s12, s1, s6
	s_ashr_i32 s13, s12, 31
	s_lshl_b64 s[12:13], s[12:13], 2
	s_add_u32 s18, s94, s12
	s_addc_u32 s19, s95, s13
	s_ashr_i32 s1, s0, 31
	s_lshl_b64 s[0:1], s[0:1], 13
	s_add_u32 s0, s92, s0
	s_addc_u32 s1, s93, s1
	s_lshl_b32 s6, s6, 8
	s_mul_i32 s20, s3, 0x3800
	s_mul_hi_u32 s21, s2, 0x3800
	s_add_u32 s0, s0, s6
	s_mul_i32 s26, s2, 0x3800
	s_addc_u32 s1, s1, 0
	s_add_i32 s21, s21, s20
	v_lshl_add_u64 v[0:1], v[230:231], 2, s[0:1]
	s_add_u32 s0, s16, s26
	s_addc_u32 s1, s17, s21
	s_lshl_b32 s28, s10, 7
	s_lshl_b32 s12, s10, 8
	s_add_u32 s0, s0, s12
	s_addc_u32 s1, s1, 0
	s_add_u32 s0, s0, 0x2400
	s_addc_u32 s1, s1, 0
	v_ashrrev_i32_e32 v6, 2, v230
	v_lshlrev_b32_e32 v102, 4, v230
	v_mov_b64_e32 v[2:3], s[0:1]
	v_and_b32_e32 v96, 48, v102
	v_mad_i64_i32 v[2:3], s[0:1], v6, s91, v[2:3]
	v_lshl_add_u64 v[14:15], v[2:3], 0, v[96:97]
	global_load_dword v96, v[0:1], off
	s_nop 0
	global_load_dwordx4 v[0:3], v[14:15], off
	global_load_dword v218, v[4:5], off offset:32
	v_lshlrev_b32_e32 v103, 2, v230
	v_add_u32_e32 v219, -4, v103
	v_add_co_u32_e32 v30, vcc, s96, v14
	v_add_u32_e32 v220, -8, v103
	s_nop 0
	v_addc_co_u32_e32 v31, vcc, 0, v15, vcc
	v_cmp_gt_i32_e32 vcc, 1, v230
	v_add_co_u32_e64 v46, s[0:1], s35, v14
	v_add_u32_e32 v104, -16, v103
	s_nop 0
	v_addc_co_u32_e64 v47, s[0:1], 0, v15, s[0:1]
	v_cmp_gt_i32_e64 s[0:1], 2, v230
	v_cmp_gt_i32_e64 s[40:41], 4, v230
	v_subrev_u32_e32 v105, 32, v103
	v_cmp_gt_i32_e64 s[46:47], 8, v230
	v_subrev_u32_e32 v106, 64, v103
	v_add_co_u32_e64 v62, s[38:39], s36, v14
	v_add_u32_e32 v107, 0xffffff80, v103
	s_nop 0
	v_addc_co_u32_e64 v63, s[38:39], 0, v15, s[38:39]
	v_cmp_gt_i32_e64 s[38:39], 16, v230
	v_mov_b32_e32 v5, s3
	v_and_or_b32 v4, v230, 31, s2
	v_lshlrev_b64 v[4:5], 10, v[4:5]
	v_and_b32_e32 v6, -8, v6
	v_lshl_add_u64 v[4:5], s[88:89], 0, v[4:5]
	v_ashrrev_i32_e32 v7, 31, v6
	v_lshl_add_u64 v[4:5], v[4:5], 0, s[28:29]
	v_lshl_add_u64 v[12:13], v[6:7], 1, v[4:5]
	global_load_dword v108, v97, s[18:19]
	global_load_dwordx4 v[64:67], v[12:13], off offset:512
	global_load_dwordx4 v[4:7], v[14:15], off offset:64
	global_load_dwordx4 v[8:11], v[14:15], off offset:128
	v_cmp_gt_i32_e64 s[42:43], 32, v230
	v_add_u32_e32 v103, s5, v103
	v_add_u32_e32 v102, s5, v102
	s_mov_b32 s6, 0
	global_load_dwordx4 v[14:17], v[14:15], off offset:192
	s_nop 0
	global_load_dwordx4 v[18:21], v[30:31], off
	global_load_dwordx4 v[22:25], v[30:31], off offset:64
	global_load_dwordx4 v[26:29], v[30:31], off offset:128
	global_load_dwordx4 v[30:33], v[30:31], off offset:192
	s_nop 0
	global_load_dwordx4 v[34:37], v[46:47], off
	global_load_dwordx4 v[38:41], v[46:47], off offset:64
	global_load_dwordx4 v[42:45], v[46:47], off offset:128
	global_load_dwordx4 v[46:49], v[46:47], off offset:192
	s_nop 0
	global_load_dwordx4 v[50:53], v[62:63], off
	global_load_dwordx4 v[54:57], v[62:63], off offset:64
	global_load_dwordx4 v[58:61], v[62:63], off offset:128
	global_load_dwordx4 v[98:101], v[62:63], off offset:192
	global_load_dwordx4 v[80:83], v[12:13], off offset:32
	global_load_dwordx4 v[84:87], v[12:13], off offset:64
	global_load_dwordx4 v[68:71], v[12:13], off offset:544
	global_load_dwordx4 v[72:75], v[12:13], off offset:576
	global_load_dwordx4 v[92:95], v[12:13], off offset:96
	global_load_dwordx4 v[76:79], v[12:13], off offset:608
	global_load_dwordx4 v[88:91], v[12:13], off
	s_waitcnt vmcnt(27)
; __device__ __forceinline__ float shfl_idx(float x, int srclane) { return __int_as_float(__builtin_amdgcn_ds_bpermute(srclane << 2, __float_as_int(x))); }
; #define LFW(off) ((__attribute__((address_space(3))) float*)(R + W_SC + (off)))
; __device__ __forceinline__ void x3_wave(int item, int b0, const h16* __restrict__ proj, const float* __restrict__ small, const h16* __restrict__ qkc, const h16* __restrict__ CS, ...
;     ...
;         float bc = lf;
; #pragma unroll
;         for (int o = 1; o < 64; o <<= 1) { const float u = shfl_idx(bc, lane - o); if (lane >= o) bc += u; }
;         const float as = li - bc; float pm = as;
; #pragma unroll
;         for (int o = 1; o < 64; o <<= 1) { const float u = shfl_idx(pm, lane - o); if (lane >= o) pm = fmaxf(pm, u); }
;         const float mx = fmaxf(Mc, pm);
;         LFW(0)[lane] = as; LFW(256)[lane] = mx; LFW(512)[lane] = __expf(Mc - mx); LFW(768)[lane] = __expf(-(bc + mx));
;         LFW(1280)[lane] = nsv;
; #pragma unroll
;         for (int sg = 0; sg < 4; ++sg)
; #pragma unroll
;             for (int vb = 0; vb < 4; ++vb) *(__attribute__((address_space(3))) h16x8*)(R + W_V + vb * 4096 + sg * 1024 + lane * 16) = xv[sg][vb];
	ds_bpermute_b32 v211, v219, v210
	s_waitcnt lgkmcnt(0)
	v_add_f32_e32 v211, v210, v211
	v_cndmask_b32_e32 v210, v211, v210, vcc
	ds_bpermute_b32 v211, v220, v210
	s_waitcnt lgkmcnt(0)
	v_add_f32_e32 v211, v210, v211
	v_cndmask_b32_e64 v210, v211, v210, s[0:1]
	ds_bpermute_b32 v211, v104, v210
	s_waitcnt lgkmcnt(0)
	v_add_f32_e32 v211, v210, v211
	v_cndmask_b32_e64 v212, v211, v210, s[40:41]
	ds_bpermute_b32 v213, v105, v212
	s_waitcnt lgkmcnt(0)
	v_add_f32_e32 v213, v212, v213
	v_cndmask_b32_e64 v214, v213, v212, s[46:47]
	ds_bpermute_b32 v215, v106, v214
	s_waitcnt lgkmcnt(0)
	v_add_f32_e32 v215, v214, v215
	v_cndmask_b32_e64 v216, v215, v214, s[38:39]
	ds_bpermute_b32 v217, v107, v216
	s_waitcnt lgkmcnt(0)
	v_add_f32_e32 v62, v216, v217
	v_cndmask_b32_e64 v62, v62, v216, s[42:43]
	s_waitcnt vmcnt(24)
	v_sub_f32_e32 v63, v218, v62
	ds_bpermute_b32 v221, v219, v63
	s_waitcnt lgkmcnt(0)
	v_max_f32_e32 v221, v221, v221
	v_max_f32_e32 v221, v63, v221
	v_cndmask_b32_e32 v109, v221, v63, vcc
	ds_bpermute_b32 v110, v220, v109
	s_waitcnt lgkmcnt(0)
	v_max_f32_e32 v12, v110, v110
	v_max_f32_e32 v12, v109, v12
	v_cndmask_b32_e64 v12, v12, v109, s[0:1]
	ds_bpermute_b32 v13, v104, v12
	s_add_u32 s0, s79, s14
	s_addc_u32 s1, s90, s15
	s_lshl_b32 s13, s10, 6
	s_add_u32 s0, s0, s11
	s_waitcnt lgkmcnt(0)
	v_max_f32_e32 v13, v13, v13
	v_max_f32_e32 v13, v12, v13
	v_cndmask_b32_e64 v12, v13, v12, s[40:41]
	ds_bpermute_b32 v13, v105, v12
	s_waitcnt vmcnt(23)
	v_max_f32_e32 v104, v108, v108
	s_addc_u32 s1, s1, 0
	s_lshl_b32 s10, s10, 9
	s_add_u32 s14, s45, s10
	s_waitcnt lgkmcnt(0)
	v_max_f32_e32 v13, v13, v13
	v_max_f32_e32 v13, v12, v13
	v_cndmask_b32_e64 v12, v13, v12, s[46:47]
	ds_bpermute_b32 v13, v106, v12
	s_addc_u32 s15, s54, 0
	v_readlane_b32 s10, v253, 58
	s_add_u32 s20, s10, s12
	v_readlane_b32 s10, v253, 59
	s_waitcnt lgkmcnt(0)
	v_max_f32_e32 v13, v13, v13
	v_max_f32_e32 v13, v12, v13
	v_cndmask_b32_e64 v12, v13, v12, s[38:39]
	ds_bpermute_b32 v13, v107, v12
	v_max_f32_e32 v105, v12, v12
	s_addc_u32 s21, s10, 0
	s_mov_b64 s[46:47], -1
	s_lshl_b32 s28, s28, 1
	s_waitcnt lgkmcnt(0)
	v_max_f32_e32 v13, v13, v13
	v_max_f32_e32 v13, v105, v13
	v_cndmask_b32_e64 v12, v13, v12, s[42:43]
	v_max_f32_e32 v12, v12, v12
	v_max_f32_e32 v12, v104, v12
	v_sub_f32_e32 v13, v108, v12
	v_add_f32_e32 v62, v62, v12
	v_mul_f32_e32 v13, 0x3fb8aa3b, v13
	v_mul_f32_e32 v62, 0xbfb8aa3b, v62
	v_exp_f32_e32 v13, v13
	v_exp_f32_e32 v62, v62
	s_lshl_b32 s40, s13, 1
	ds_write_b32 v103, v96 offset:26368
	ds_write2st64_b32 v103, v63, v12 offset0:98 offset1:99
	ds_write2st64_b32 v103, v13, v62 offset0:100 offset1:101
	ds_write_b128 v102, v[0:3]
	s_waitcnt vmcnt(21)
	ds_write_b128 v102, v[4:7] offset:4096
	s_waitcnt vmcnt(20)
	ds_write_b128 v102, v[8:11] offset:8192
	s_waitcnt vmcnt(19)
	ds_write_b128 v102, v[14:17] offset:12288
	s_waitcnt vmcnt(18)
	ds_write_b128 v102, v[18:21] offset:1024
	s_waitcnt vmcnt(17)
	ds_write_b128 v102, v[22:25] offset:5120
	s_waitcnt vmcnt(16)
	ds_write_b128 v102, v[26:29] offset:9216
	s_waitcnt vmcnt(15)
	ds_write_b128 v102, v[30:33] offset:13312
	s_waitcnt vmcnt(14)
	ds_write_b128 v102, v[34:37] offset:2048
	s_waitcnt vmcnt(13)
	ds_write_b128 v102, v[38:41] offset:6144
	s_waitcnt vmcnt(12)
	ds_write_b128 v102, v[42:45] offset:10240
	s_waitcnt vmcnt(11)
	ds_write_b128 v102, v[46:49] offset:14336
	s_waitcnt vmcnt(10)
	ds_write_b128 v102, v[50:53] offset:3072
	s_waitcnt vmcnt(9)
	ds_write_b128 v102, v[54:57] offset:7168
	s_waitcnt vmcnt(8)
	ds_write_b128 v102, v[58:61] offset:11264
	s_waitcnt vmcnt(7)
	ds_write_b128 v102, v[98:101] offset:15360
	s_waitcnt lgkmcnt(0)
	v_mov_b64_e32 v[100:101], v[66:67]
	v_mov_b64_e32 v[98:99], v[64:65]
	s_waitcnt vmcnt(4)
	v_mov_b64_e32 v[104:105], v[70:71]
	s_waitcnt vmcnt(3)
	v_mov_b64_e32 v[108:109], v[74:75]
	v_mov_b64_e32 v[102:103], v[68:69]
	v_mov_b64_e32 v[106:107], v[72:73]
	s_waitcnt vmcnt(1)
	v_mov_b64_e32 v[112:113], v[78:79]
	v_mov_b64_e32 v[110:111], v[76:77]
	s_branch .LBB0_431
